# one shared token-list table per step written four blocks ahead by a rotating wave; block-major steps look lists up instead of recomputing masks and ranks
# baseline (speedup 1.0000x reference)
.LBB0_1185:
	s_cmp_lt_u32 s75, 2
	s_cbranch_scc0 .Lbm_hk_ge2
	s_cmp_gt_u32 s91, 1
	s_cbranch_scc1 .Lbm_old
	s_lshl_b32 s77, s91, 1
	s_add_i32 s77, s77, 2
	s_cmp_gt_i32 s77, s26
	s_cbranch_scc1 .Lbm_old
	s_lshr_b32 s83, s77, 1
	s_and_b32 s83, s83, 3
	s_mul_i32 s83, s83, 80
	s_add_i32 s83, s83, 0x20900
	s_lshr_b32 s21, s77, 5
	v_mov_b32_e32 v255, v242
	s_cmp_eq_u32 s21, 1
	s_cselect_b64 vcc, -1, 0
	v_cndmask_b32_e32 v255, v255, v243, vcc
	s_cmp_eq_u32 s21, 2
	s_cselect_b64 vcc, -1, 0
	v_cndmask_b32_e32 v255, v255, v244, vcc
	s_cmp_eq_u32 s21, 3
	s_cselect_b64 vcc, -1, 0
	v_cndmask_b32_e32 v255, v255, v245, vcc
	s_and_b32 s21, s77, 31
	s_lshl_b32 s21, 1, s21
	s_lshl_b32 s32, s21, 1
	v_and_b32_e32 v80, s21, v255
	v_cmp_ne_u32_e64 s[12:13], 0, v80
	v_and_b32_e32 v80, s32, v255
	v_cmp_ne_u32_e64 s[14:15], 0, v80
	s_nop 3
	s_or_b64 s[22:23], s[12:13], s[14:15]
	s_bcnt1_i32_b64 s11, s[22:23]
	s_add_i32 s11, s11, 3
	s_lshr_b32 s11, s11, 2
	s_andn2_b64 s[84:85], s[12:13], s[14:15]
	s_bcnt1_i32_b64 s77, s[84:85]
	v_mbcnt_lo_u32_b32 v80, s84, 0
	v_mbcnt_hi_u32_b32 v80, s85, v80
	v_mov_b32_e32 v255, s77
	s_and_b64 s[84:85], s[12:13], s[14:15]
	s_bcnt1_i32_b64 s32, s[84:85]
	v_mbcnt_lo_u32_b32 v255, s84, v255
	v_mbcnt_hi_u32_b32 v255, s85, v255
	s_add_i32 s77, s77, s32
	v_cndmask_b32_e64 v80, v80, v255, s[84:85]
	v_mov_b32_e32 v255, s77
	s_andn2_b64 s[84:85], s[14:15], s[12:13]
	v_mbcnt_lo_u32_b32 v255, s84, v255
	v_mbcnt_hi_u32_b32 v255, s85, v255
	s_nop 0
	v_cndmask_b32_e64 v80, v80, v255, s[84:85]
	v_cndmask_b32_e64 v78, 0, 1, s[12:13]
	v_cndmask_b32_e64 v255, 0, 2, s[14:15]
	v_or_b32_e32 v78, v78, v255
	v_and_b32_e32 v255, 63, v185
	v_lshl_or_b32 v78, v78, 6, v255
	v_add_u32_e32 v255, s83, v80
	s_and_saveexec_b64 s[84:85], s[22:23]
	ds_write_b8 v255, v78
	s_mov_b64 exec, s[84:85]
	s_bcnt1_i32_b64 s32, s[22:23]
	v_mov_b32_e32 v78, s32
	v_mov_b32_e32 v255, s83
	ds_write_b8 v255, v78 offset:64
	s_branch .Lbm_old
.Lbm_hk_ge2:
	s_cmp_gt_i32 s75, s26
	s_cbranch_scc0 .Lbm_step
	s_cmp_eq_u32 s98, 0
	s_cbranch_scc1 .Lbm_old
	s_mul_i32 s11, s91, 8320
	v_mul_u32_u24_e32 v79, 260, v250
	v_add3_u32 v79, v79, s11, v248
	v_lshlrev_b32_e32 v80, 6, v186
	v_sub_u32_e32 v80, v79, v80
	ds_read_b32 v70, v79 offset:0
	ds_read_b32 v71, v79 offset:16
	ds_read_b32 v72, v79 offset:32
	ds_read_b32 v73, v79 offset:48
	ds_read_b32 v66, v79 offset:256
	ds_read_b32 v67, v79 offset:272
	ds_read_b32 v68, v79 offset:288
	ds_read_b32 v69, v79 offset:304
	ds_read_b32 v62, v79 offset:512
	ds_read_b32 v63, v79 offset:528
	ds_read_b32 v64, v79 offset:544
	ds_read_b32 v65, v79 offset:560
	s_waitcnt lgkmcnt(0)
	ds_read_b32 v54, v79 offset:768
	ds_read_b32 v55, v79 offset:784
	ds_read_b32 v56, v79 offset:800
	ds_read_b32 v57, v79 offset:816
	ds_read_b32 v50, v79 offset:4160
	ds_read_b32 v51, v79 offset:4176
	ds_read_b32 v52, v79 offset:4192
	ds_read_b32 v53, v79 offset:4208
	ds_read_b32 v46, v79 offset:4416
	ds_read_b32 v47, v79 offset:4432
	ds_read_b32 v48, v79 offset:4448
	ds_read_b32 v49, v79 offset:4464
	s_waitcnt lgkmcnt(0)
	ds_read_b32 v42, v79 offset:4672
	ds_read_b32 v43, v79 offset:4688
	ds_read_b32 v44, v79 offset:4704
	ds_read_b32 v45, v79 offset:4720
	ds_read_b32 v38, v79 offset:4928
	ds_read_b32 v39, v79 offset:4944
	ds_read_b32 v40, v79 offset:4960
	ds_read_b32 v41, v79 offset:4976
	ds_read_b32 v74, v80 offset:1024
	ds_read_b32 v58, v80 offset:5184
	s_waitcnt lgkmcnt(0)
	v_mov_b32_e32 v75, v74
	v_mov_b32_e32 v76, v74
	v_mov_b32_e32 v77, v74
	v_mov_b32_e32 v59, v58
	v_mov_b32_e32 v60, v58
	v_mov_b32_e32 v61, v58
	s_bitcmp1_b32 s26, 0
	s_cbranch_scc1 .Lbm_hk4
	s_waitcnt vmcnt(2)
	s_branch .Lbm_hkd

.Lbm_step:
	s_mov_b32 s98, 1
	s_lshr_b32 s11, s75, 1
	s_and_b32 s11, s11, 7
	s_cmp_lg_u32 s11, s91
	s_cbranch_scc1 .Lbm_noprod
	s_add_i32 s77, s75, 4
	s_cmp_gt_i32 s77, s26
	s_cbranch_scc1 .Lbm_noprod
	s_lshr_b32 s83, s77, 1
	s_and_b32 s83, s83, 3
	s_mul_i32 s83, s83, 80
	s_add_i32 s83, s83, 0x20900
	s_lshr_b32 s21, s77, 5
	v_mov_b32_e32 v255, v242
	s_cmp_eq_u32 s21, 1
	s_cselect_b64 vcc, -1, 0
	v_cndmask_b32_e32 v255, v255, v243, vcc
	s_cmp_eq_u32 s21, 2
	s_cselect_b64 vcc, -1, 0
	v_cndmask_b32_e32 v255, v255, v244, vcc
	s_cmp_eq_u32 s21, 3
	s_cselect_b64 vcc, -1, 0
	v_cndmask_b32_e32 v255, v255, v245, vcc
	s_and_b32 s21, s77, 31
	s_lshl_b32 s21, 1, s21
	s_lshl_b32 s32, s21, 1
	v_and_b32_e32 v80, s21, v255
	v_cmp_ne_u32_e64 s[12:13], 0, v80
	v_and_b32_e32 v80, s32, v255
	v_cmp_ne_u32_e64 s[14:15], 0, v80
	s_nop 3
	s_or_b64 s[22:23], s[12:13], s[14:15]
	s_bcnt1_i32_b64 s11, s[22:23]
	s_add_i32 s11, s11, 3
	s_lshr_b32 s11, s11, 2
	s_andn2_b64 s[84:85], s[12:13], s[14:15]
	s_bcnt1_i32_b64 s77, s[84:85]
	v_mbcnt_lo_u32_b32 v80, s84, 0
	v_mbcnt_hi_u32_b32 v80, s85, v80
	v_mov_b32_e32 v255, s77
	s_and_b64 s[84:85], s[12:13], s[14:15]
	s_bcnt1_i32_b64 s32, s[84:85]
	v_mbcnt_lo_u32_b32 v255, s84, v255
	v_mbcnt_hi_u32_b32 v255, s85, v255
	s_add_i32 s77, s77, s32
	v_cndmask_b32_e64 v80, v80, v255, s[84:85]
	v_mov_b32_e32 v255, s77
	s_andn2_b64 s[84:85], s[14:15], s[12:13]
	v_mbcnt_lo_u32_b32 v255, s84, v255
	v_mbcnt_hi_u32_b32 v255, s85, v255
	s_nop 0
	v_cndmask_b32_e64 v80, v80, v255, s[84:85]
	v_cndmask_b32_e64 v78, 0, 1, s[12:13]
	v_cndmask_b32_e64 v255, 0, 2, s[14:15]
	v_or_b32_e32 v78, v78, v255
	v_and_b32_e32 v255, 63, v185
	v_lshl_or_b32 v78, v78, 6, v255
	v_add_u32_e32 v255, s83, v80
	s_and_saveexec_b64 s[84:85], s[22:23]
	ds_write_b8 v255, v78
	s_mov_b64 exec, s[84:85]
	s_bcnt1_i32_b64 s32, s[22:23]
	v_mov_b32_e32 v78, s32
	v_mov_b32_e32 v255, s83
	ds_write_b8 v255, v78 offset:64
.Lbm_noprod:
	s_cmp_eq_u32 s100, s75
	s_cbranch_scc0 .Lbm_slow
	s_and_b32 s83, s1, 0x4000
	v_mov_b32_e32 v112, s20
	v_mov_b32_e32 v113, s20
	v_mov_b32_e32 v114, s20
	v_mov_b32_e32 v115, s20
	v_lshrrev_b32_e32 v56, 31, v251
	v_xor_b32_e32 v56, 1, v56
	v_max_i32_e32 v55, 0, v251
	v_mov_b32_e32 v79, v56
	v_and_b32_e32 v54, 63, v55
	v_bfe_u32 v58, v55, 6, 1
	v_bfe_u32 v59, v55, 7, 1
	v_lshl_add_u32 v63, v54, 4, v249
	ds_read_b32 v199, v63
	v_mul_u32_u24_e32 v83, 0x410, v54
	v_cmp_ne_u32_e32 vcc, 0, v58
	v_add_u32_e32 v83, v83, v248
	s_nop 0
	v_cndmask_b32_e32 v81, v2, v154, vcc
	s_cmp_lg_u64 vcc, 0
	s_cselect_b32 s21, 1, 0
	v_cmp_ne_u32_e32 vcc, 0, v59
	s_nop 1
	v_cndmask_b32_e32 v82, v2, v154, vcc
	s_cmp_lg_u64 vcc, 0
	s_cselect_b32 s32, 1, 0
	s_cmp_eq_u32 s101, 4
	s_cbranch_scc1 .Lbm_q4_f
	s_cmp_eq_u32 s101, 8
	s_cbranch_scc1 .Lbm_q8_f
	s_waitcnt vmcnt(0)
	s_branch .Lbm_qd_f

; __device__ __forceinline__ float ex2(float x) { return __builtin_amdgcn_exp2f(x); }
; template <int C>
; __device__ __forceinline__ void attn_far1_fast(const LAS unsigned char* kb, const LAS unsigned char* vb, const bf16x8 (&qf)[2][2], int col, int q, float bias_far, bool sel, Softmax (&st)[2], f32x4 (&O)[2][4]) {
;     ...
; #pragma unroll
;     for (int kt = 0; kt < 4; ++kt) { const bf16x8 k0 = lds_frag(kb, 16 * kt + col, q), k1 = lds_frag(kb, 16 * kt + col, 4 + q);
;         S[kt] = __builtin_amdgcn_mfma_f32_16x16x32_bf16(k0, qf[C][0], z4, 0, 0, 0); S[kt] = __builtin_amdgcn_mfma_f32_16x16x32_bf16(k1, qf[C][1], S[kt], 0, 0, 0); }
;     const float off = (sel ? bias_far : NEG) - st[C].m;
; #pragma unroll
;     for (int kt = 0; kt < 4; ++kt) { f32x4 p = S[kt] + off;
; #pragma unroll
;         for (int e = 0; e < 4; ++e) p[e] = ex2(p[e]);
;         S[kt] = p; }
;     const bf16x8 pf0 = pack8(S[0], S[1]), pf1 = pack8(S[2], S[3]);
;     st[C].l = __builtin_amdgcn_mfma_f32_16x16x32_bf16(ONES8, pf0, st[C].l, 0, 0, 0); st[C].l = __builtin_amdgcn_mfma_f32_16x16x32_bf16(ONES8, pf1, st[C].l, 0, 0, 0);
; #pragma unroll
;     for (int dt = 0; dt < 4; ++dt) { const bf16x8 vf0 = lds_frag(vb, 16 * dt + col, q), vf1 = lds_frag(vb, 16 * dt + col, 4 + q);
;         O[C][dt] = __builtin_amdgcn_mfma_f32_16x16x32_bf16(vf0, pf0, O[C][dt], 0, 0, 0); O[C][dt] = __builtin_amdgcn_mfma_f32_16x16x32_bf16(vf1, pf1, O[C][dt], 0, 0, 0); }
; }
.Lbm_half_f:
	v_add_u32_e32 v148, s77, v192
	v_add_u32_e32 v149, v148, v195
	v_add_u32_e32 v148, v148, v193
	ds_read_b128 v[116:119], v148
	ds_read_b128 v[120:123], v149
	ds_read_b128 v[124:127], v148 offset:2048
	ds_read_b128 v[128:131], v149 offset:2048
	ds_read_b128 v[132:135], v148 offset:4096
	ds_read_b128 v[136:139], v149 offset:4096
	ds_read_b128 v[140:143], v148 offset:6144
	ds_read_b128 v[144:147], v149 offset:6144
	s_waitcnt lgkmcnt(8)
	v_sub_f32_e32 v81, v81, v199
	v_sub_f32_e32 v82, v82, v199
	v_mov_b32_e32 v54, v81
	v_mov_b32_e32 v55, v81
	v_mov_b32_e32 v56, v81
	v_mov_b32_e32 v57, v81
	s_mov_b32 s83, -1
	s_add_i32 s77, s75, 2
	s_cmp_gt_i32 s77, s26
	s_cbranch_scc1 .Lbm_g1_end_hf
	s_lshr_b32 s77, s77, 1
	s_and_b32 s77, s77, 3
	s_mul_i32 s77, s77, 80
	s_add_i32 s77, s77, 0x20900
	s_lshl_b32 s32, s91, 2
	v_lshrrev_b32_e32 v78, 2, v250
	v_add_u32_e32 v78, s32, v78
	v_mov_b32_e32 v255, s77
	v_add_u32_e32 v254, s77, v78
	ds_read_u8 v255, v255 offset:64
	ds_read_u8 v251, v254
	s_mov_b32 s83, 0
.Lbm_g1_end_hf:
	s_waitcnt lgkmcnt(6)
	v_mfma_f32_16x16x32_bf16 v[70:73], v[116:119], v[104:107], v[54:57]
	v_mfma_f32_16x16x32_bf16 v[70:73], v[120:123], v[108:111], v[70:73]
	s_waitcnt lgkmcnt(4)
	v_mfma_f32_16x16x32_bf16 v[74:77], v[124:127], v[104:107], v[54:57]
	v_mfma_f32_16x16x32_bf16 v[74:77], v[128:131], v[108:111], v[74:77]
	ds_read_b128 v[116:119], v148 offset:32768
	ds_read_b128 v[120:123], v149 offset:32768
	ds_read_b128 v[124:127], v148 offset:34816
	ds_read_b128 v[128:131], v149 offset:34816
	s_waitcnt lgkmcnt(6)
	v_mfma_f32_16x16x32_bf16 v[200:203], v[132:135], v[104:107], v[54:57]
	v_mfma_f32_16x16x32_bf16 v[200:203], v[136:139], v[108:111], v[200:203]
	s_waitcnt lgkmcnt(4)
	v_mfma_f32_16x16x32_bf16 v[204:207], v[140:143], v[104:107], v[54:57]
	v_mfma_f32_16x16x32_bf16 v[204:207], v[144:147], v[108:111], v[204:207]
	ds_read_b128 v[132:135], v148 offset:36864
	ds_read_b128 v[136:139], v149 offset:36864
	ds_read_b128 v[140:143], v148 offset:38912
	ds_read_b128 v[144:147], v149 offset:38912
	s_mov_b32 s100, -1
	s_cmp_lt_i32 s83, 0
	s_cbranch_scc1 .Lbm_g2_end_hf
	s_waitcnt lgkmcnt(8)
	v_readfirstlane_b32 s11, v255
	s_add_i32 s32, s11, 3
	s_lshr_b32 s32, s32, 2
	s_cmp_ge_u32 s91, s32
	s_cbranch_scc1 .Lbm_g2_end_hf
	v_cmp_gt_u32_e32 vcc, s11, v78
	s_add_i32 s83, s91, 8
	s_cmp_lt_u32 s83, s32
	s_cselect_b32 s83, 0x10000, 0
	s_add_i32 s83, s83, s75
	s_add_i32 s83, s83, 2
	v_cndmask_b32_e32 v251, -1, v251, vcc
	v_max_i32_e32 v254, 0, v251
	v_and_b32_e32 v254, 63, v254
	v_lshlrev_b32_e32 v254, 11, v254
	v_mov_b32_e32 v255, 0
	v_lshl_add_u64 v[254:255], v[254:255], 0, v[246:247]
	global_load_dwordx4 v[104:107], v[254:255], off
	global_load_dwordx4 v[108:111], v[254:255], off offset:64
	s_mov_b32 s100, s83

; __device__ __forceinline__ float ex2(float x) { return __builtin_amdgcn_exp2f(x); }
; template <bool SELMASK>
; __device__ __forceinline__ void attn_far_fast(const LAS unsigned char* kb, const LAS unsigned char* vb, const bf16x8 (&qf)[2][2], int col, int q, float bias_far, bool sel0, bool sel1, Softmax (&st)[2], f32x4 (&O)[2][4]) {
;     ...
; #pragma unroll
;     for (int kt = 0; kt < 4; ++kt) { const bf16x8 k0 = lds_frag(kb, 16 * kt + col, q), k1 = lds_frag(kb, 16 * kt + col, 4 + q);
; #pragma unroll
;         for (int c = 0; c < 2; ++c) { S[c][kt] = __builtin_amdgcn_mfma_f32_16x16x32_bf16(k0, qf[c][0], z4, 0, 0, 0); S[c][kt] = __builtin_amdgcn_mfma_f32_16x16x32_bf16(k1, qf[c][1], S[c][kt], 0, 0, 0); } }
;     bf16x8 pf[2][2];
; #pragma unroll
;     for (int c = 0; c < 2; ++c) {
;         const bool sel = c == 0 ? sel0 : sel1;
;         const float off = ((SELMASK && !sel) ? NEG : bias_far) - st[c].m;
; #pragma unroll
;         for (int kt = 0; kt < 4; ++kt) { f32x4 p = S[c][kt] + off;
; #pragma unroll
;             for (int e = 0; e < 4; ++e) p[e] = ex2(p[e]);
;             S[c][kt] = p; }
;         pf[c][0] = pack8(S[c][0], S[c][1]); pf[c][1] = pack8(S[c][2], S[c][3]);
;         st[c].l = __builtin_amdgcn_mfma_f32_16x16x32_bf16(ONES8, pf[c][0], st[c].l, 0, 0, 0); st[c].l = __builtin_amdgcn_mfma_f32_16x16x32_bf16(ONES8, pf[c][1], st[c].l, 0, 0, 0);
;     }
.Lbm_full_f:
	v_add_u32_e32 v148, s83, v192
	v_add_u32_e32 v149, v148, v195
	v_add_u32_e32 v148, v148, v193
	ds_read_b128 v[116:119], v148
	ds_read_b128 v[120:123], v149
	ds_read_b128 v[124:127], v148 offset:2048
	ds_read_b128 v[128:131], v149 offset:2048
	ds_read_b128 v[132:135], v148 offset:4096
	ds_read_b128 v[136:139], v149 offset:4096
	ds_read_b128 v[140:143], v148 offset:6144
	ds_read_b128 v[144:147], v149 offset:6144
	s_add_i32 s32, s1, 0x2000
	s_and_b32 s32, s32, 0x6000
	v_add_u32_e32 v208, s32, v192
	v_add_u32_e32 v209, v208, v195
	v_add_u32_e32 v208, v208, v193
	ds_read_b128 v[38:41], v208
	ds_read_b128 v[42:45], v209
	ds_read_b128 v[46:49], v208 offset:2048
	ds_read_b128 v[50:53], v209 offset:2048
	s_waitcnt lgkmcnt(12)
	v_sub_f32_e32 v81, v81, v199
	v_sub_f32_e32 v82, v82, v199
	v_mov_b32_e32 v70, v81
	v_mov_b32_e32 v71, v81
	v_mov_b32_e32 v72, v81
	v_mov_b32_e32 v73, v81
	v_mov_b32_e32 v74, v81
	v_mov_b32_e32 v75, v81
	v_mov_b32_e32 v76, v81
	v_mov_b32_e32 v77, v81
	v_mov_b32_e32 v200, v81
	v_mov_b32_e32 v201, v81
	v_mov_b32_e32 v202, v81
	v_mov_b32_e32 v203, v81
	v_mov_b32_e32 v204, v81
	v_mov_b32_e32 v205, v81
	v_mov_b32_e32 v206, v81
	v_mov_b32_e32 v207, v81
	v_mov_b32_e32 v54, v82
	v_mov_b32_e32 v55, v82
	v_mov_b32_e32 v56, v82
	v_mov_b32_e32 v57, v82
	v_mov_b32_e32 v58, v82
	v_mov_b32_e32 v59, v82
	v_mov_b32_e32 v60, v82
	v_mov_b32_e32 v61, v82
	v_mov_b32_e32 v62, v82
	v_mov_b32_e32 v63, v82
	v_mov_b32_e32 v64, v82
	v_mov_b32_e32 v65, v82
	v_mov_b32_e32 v66, v82
	v_mov_b32_e32 v67, v82
	v_mov_b32_e32 v68, v82
	v_mov_b32_e32 v69, v82
	s_mov_b32 s83, -1
	s_add_i32 s77, s75, 2
	s_cmp_gt_i32 s77, s26
	s_cbranch_scc1 .Lbm_g1_end_af
	s_lshr_b32 s77, s77, 1
	s_and_b32 s77, s77, 3
	s_mul_i32 s77, s77, 80
	s_add_i32 s77, s77, 0x20900
	s_lshl_b32 s32, s91, 2
	v_lshrrev_b32_e32 v78, 2, v250
	v_add_u32_e32 v78, s32, v78
	v_mov_b32_e32 v255, s77
	v_add_u32_e32 v254, s77, v78
	ds_read_u8 v255, v255 offset:64
	ds_read_u8 v251, v254
	s_mov_b32 s83, 0
.Lbm_g1_end_af:
	s_waitcnt lgkmcnt(10)
	v_mfma_f32_16x16x32_bf16 v[70:73], v[116:119], v[104:107], v[70:73]
	v_mfma_f32_16x16x32_bf16 v[70:73], v[120:123], v[108:111], v[70:73]
	s_waitcnt lgkmcnt(8)
	v_mfma_f32_16x16x32_bf16 v[74:77], v[124:127], v[104:107], v[74:77]
	v_mfma_f32_16x16x32_bf16 v[74:77], v[128:131], v[108:111], v[74:77]
	ds_read_b128 v[116:119], v148 offset:32768
	ds_read_b128 v[120:123], v149 offset:32768
	ds_read_b128 v[124:127], v148 offset:34816
	ds_read_b128 v[128:131], v149 offset:34816
	s_waitcnt lgkmcnt(10)
	v_mfma_f32_16x16x32_bf16 v[200:203], v[132:135], v[104:107], v[200:203]
	v_mfma_f32_16x16x32_bf16 v[200:203], v[136:139], v[108:111], v[200:203]
	s_waitcnt lgkmcnt(8)
	v_mfma_f32_16x16x32_bf16 v[204:207], v[140:143], v[104:107], v[204:207]
	v_mfma_f32_16x16x32_bf16 v[204:207], v[144:147], v[108:111], v[204:207]
	ds_read_b128 v[132:135], v148 offset:36864
	ds_read_b128 v[136:139], v149 offset:36864
	ds_read_b128 v[140:143], v148 offset:38912
	ds_read_b128 v[144:147], v149 offset:38912
	s_waitcnt lgkmcnt(10)
	v_mfma_f32_16x16x32_bf16 v[54:57], v[38:41], v[104:107], v[54:57]
	v_mfma_f32_16x16x32_bf16 v[54:57], v[42:45], v[108:111], v[54:57]
	s_waitcnt lgkmcnt(8)
	v_mfma_f32_16x16x32_bf16 v[58:61], v[46:49], v[104:107], v[58:61]
	v_mfma_f32_16x16x32_bf16 v[58:61], v[50:53], v[108:111], v[58:61]
	ds_read_b128 v[38:41], v208 offset:4096
	ds_read_b128 v[42:45], v209 offset:4096
	ds_read_b128 v[46:49], v208 offset:6144
	ds_read_b128 v[50:53], v209 offset:6144
	v_exp_f32_e32 v70, v70
	v_exp_f32_e32 v71, v71
	v_exp_f32_e32 v72, v72
	v_exp_f32_e32 v73, v73
	v_exp_f32_e32 v74, v74
	v_exp_f32_e32 v75, v75
	v_exp_f32_e32 v76, v76
	v_exp_f32_e32 v77, v77
	v_exp_f32_e32 v200, v200
	v_exp_f32_e32 v201, v201
	v_exp_f32_e32 v202, v202
	v_exp_f32_e32 v203, v203
	v_exp_f32_e32 v204, v204
	v_exp_f32_e32 v205, v205
	v_exp_f32_e32 v206, v206
	v_exp_f32_e32 v207, v207
	s_nop 0
	v_cvt_pk_bf16_f32 v70, v70, v71
	v_cvt_pk_bf16_f32 v71, v72, v73
	v_cvt_pk_bf16_f32 v72, v74, v75
	v_cvt_pk_bf16_f32 v73, v76, v77
	v_cvt_pk_bf16_f32 v74, v200, v201
	v_cvt_pk_bf16_f32 v75, v202, v203
	v_cvt_pk_bf16_f32 v76, v204, v205
	v_cvt_pk_bf16_f32 v77, v206, v207
	s_nop 1
	v_mfma_f32_16x16x32_bf16 v[100:103], v[112:115], v[70:73], 0
	v_mfma_f32_16x16x32_bf16 v[100:103], v[112:115], v[74:77], v[100:103]
	s_waitcnt lgkmcnt(4)
	v_mfma_f32_16x16x32_bf16 v[84:87], v[116:119], v[70:73], 0
	v_mfma_f32_16x16x32_bf16 v[84:87], v[120:123], v[74:77], v[84:87]
	v_mfma_f32_16x16x32_bf16 v[88:91], v[124:127], v[70:73], 0
	v_mfma_f32_16x16x32_bf16 v[88:91], v[128:131], v[74:77], v[88:91]
	v_mfma_f32_16x16x32_bf16 v[92:95], v[132:135], v[70:73], 0
	v_mfma_f32_16x16x32_bf16 v[92:95], v[136:139], v[74:77], v[92:95]
	v_mfma_f32_16x16x32_bf16 v[96:99], v[140:143], v[70:73], 0
	v_mfma_f32_16x16x32_bf16 v[96:99], v[144:147], v[74:77], v[96:99]
	s_waitcnt lgkmcnt(2)
	v_mfma_f32_16x16x32_bf16 v[62:65], v[38:41], v[104:107], v[62:65]
	v_mfma_f32_16x16x32_bf16 v[62:65], v[42:45], v[108:111], v[62:65]
	s_waitcnt lgkmcnt(0)
	v_mfma_f32_16x16x32_bf16 v[66:69], v[46:49], v[104:107], v[66:69]
	v_mfma_f32_16x16x32_bf16 v[66:69], v[50:53], v[108:111], v[66:69]
	ds_read_b128 v[116:119], v208 offset:32768
	ds_read_b128 v[120:123], v209 offset:32768
	ds_read_b128 v[124:127], v208 offset:34816
	ds_read_b128 v[128:131], v209 offset:34816
	ds_read_b128 v[132:135], v208 offset:36864
	ds_read_b128 v[136:139], v209 offset:36864
	ds_read_b128 v[140:143], v208 offset:38912
	ds_read_b128 v[144:147], v209 offset:38912
	s_mov_b32 s100, -1
	s_cmp_lt_i32 s83, 0
	s_cbranch_scc1 .Lbm_g2_end_af
	s_waitcnt lgkmcnt(8)
	v_readfirstlane_b32 s11, v255
	s_add_i32 s32, s11, 3
	s_lshr_b32 s32, s32, 2
	s_cmp_ge_u32 s91, s32
	s_cbranch_scc1 .Lbm_g2_end_af
	v_cmp_gt_u32_e32 vcc, s11, v78
	s_add_i32 s83, s91, 8
	s_cmp_lt_u32 s83, s32
	s_cselect_b32 s83, 0x10000, 0
	s_add_i32 s83, s83, s75
	s_add_i32 s83, s83, 2
	v_cndmask_b32_e32 v251, -1, v251, vcc
	v_max_i32_e32 v254, 0, v251
	v_and_b32_e32 v254, 63, v254
	v_lshlrev_b32_e32 v254, 11, v254
	v_mov_b32_e32 v255, 0
	v_lshl_add_u64 v[254:255], v[254:255], 0, v[246:247]
	global_load_dwordx4 v[104:107], v[254:255], off
	global_load_dwordx4 v[108:111], v[254:255], off offset:64
	s_mov_b32 s100, s83

.Lbm_slow:
	s_lshr_b32 s77, s75, 1
	s_and_b32 s77, s77, 3
	s_mul_i32 s77, s77, 80
	s_add_i32 s77, s77, 0x20900
	s_lshl_b32 s32, s91, 2
	v_lshrrev_b32_e32 v58, 2, v250
	v_add_u32_e32 v58, s32, v58
	v_mov_b32_e32 v59, s77
	v_add_u32_e32 v63, s77, v58
	ds_read_u8 v59, v59 offset:64
	ds_read_u8 v63, v63
	s_and_b32 s83, s1, 0x4000
	v_mov_b32_e32 v112, s20
	v_mov_b32_e32 v113, s20
	v_mov_b32_e32 v114, s20
	v_mov_b32_e32 v115, s20
	s_waitcnt lgkmcnt(0)
	v_readfirstlane_b32 s11, v59
	s_add_i32 s21, s11, 3
	s_lshr_b32 s21, s21, 2
	s_cmp_ge_u32 s91, s21
	s_cbranch_scc1 .Lbm_noitem
	v_cmp_gt_u32_e32 vcc, s11, v58
	s_add_i32 s10, s91, 8
	s_cmp_lt_u32 s10, s21
	s_cselect_b32 s10, 1, 0
	s_and_b32 s77, s100, 0xffff
	s_cmp_eq_u32 s77, s75
	s_cbranch_scc1 .Lbm_r1_pf
	v_cndmask_b32_e32 v63, -1, v63, vcc
	v_lshrrev_b32_e32 v56, 31, v63
	v_xor_b32_e32 v56, 1, v56
	v_max_i32_e32 v55, 0, v63
	v_mov_b32_e32 v79, v56
	v_and_b32_e32 v54, 63, v55
	v_bfe_u32 v58, v55, 6, 1
	v_bfe_u32 v59, v55, 7, 1
	v_lshlrev_b32_e32 v60, 11, v54
	v_mov_b32_e32 v61, 0
	v_lshl_add_u64 v[60:61], v[60:61], 0, v[246:247]
	global_load_dwordx4 v[104:107], v[60:61], off
	global_load_dwordx4 v[108:111], v[60:61], off offset:64
	v_lshl_add_u32 v63, v54, 4, v249
	ds_read_b32 v199, v63
	v_mul_u32_u24_e32 v83, 0x410, v54
	v_cmp_ne_u32_e32 vcc, 0, v58
	v_add_u32_e32 v83, v83, v248
	s_nop 0
	v_cndmask_b32_e32 v81, v2, v154, vcc
	s_cmp_lg_u64 vcc, 0
	s_cselect_b32 s21, 1, 0
	v_cmp_ne_u32_e32 vcc, 0, v59
	s_nop 1
	v_cndmask_b32_e32 v82, v2, v154, vcc
	s_cmp_lg_u64 vcc, 0
	s_cselect_b32 s32, 1, 0
	s_waitcnt vmcnt(0)
	s_branch .Lbm_r1_go

; __device__ __forceinline__ float ex2(float x) { return __builtin_amdgcn_exp2f(x); }
; template <bool SELMASK>
; __device__ __forceinline__ void attn_far_fast(const LAS unsigned char* kb, const LAS unsigned char* vb, const bf16x8 (&qf)[2][2], int col, int q, float bias_far, bool sel0, bool sel1, Softmax (&st)[2], f32x4 (&O)[2][4]) {
;     ...
; #pragma unroll
;     for (int kt = 0; kt < 4; ++kt) { const bf16x8 k0 = lds_frag(kb, 16 * kt + col, q), k1 = lds_frag(kb, 16 * kt + col, 4 + q);
; #pragma unroll
;         for (int c = 0; c < 2; ++c) { S[c][kt] = __builtin_amdgcn_mfma_f32_16x16x32_bf16(k0, qf[c][0], z4, 0, 0, 0); S[c][kt] = __builtin_amdgcn_mfma_f32_16x16x32_bf16(k1, qf[c][1], S[c][kt], 0, 0, 0); } }
;     bf16x8 pf[2][2];
; #pragma unroll
;     for (int c = 0; c < 2; ++c) {
;         const bool sel = c == 0 ? sel0 : sel1;
;         const float off = ((SELMASK && !sel) ? NEG : bias_far) - st[c].m;
; #pragma unroll
;         for (int kt = 0; kt < 4; ++kt) { f32x4 p = S[c][kt] + off;
; #pragma unroll
;             for (int e = 0; e < 4; ++e) p[e] = ex2(p[e]);
;             S[c][kt] = p; }
;         pf[c][0] = pack8(S[c][0], S[c][1]); pf[c][1] = pack8(S[c][2], S[c][3]);
;         st[c].l = __builtin_amdgcn_mfma_f32_16x16x32_bf16(ONES8, pf[c][0], st[c].l, 0, 0, 0); st[c].l = __builtin_amdgcn_mfma_f32_16x16x32_bf16(ONES8, pf[c][1], st[c].l, 0, 0, 0);
;     }
; #pragma unroll
;     for (int c32 = 0; c32 < 2; ++c32)
; #pragma unroll
;         for (int dt = 0; dt < 4; ++dt) { const bf16x8 vf = lds_frag(vb, 16 * dt + col, 4 * c32 + q);
;             O[0][dt] = __builtin_amdgcn_mfma_f32_16x16x32_bf16(vf, pf[0][c32], O[0][dt], 0, 0, 0);
;             O[1][dt] = __builtin_amdgcn_mfma_f32_16x16x32_bf16(vf, pf[1][c32], O[1][dt], 0, 0, 0); }
.Lbm_r1_two:
	v_add_u32_e32 v148, s83, v192
	v_add_u32_e32 v149, v148, v195
	v_add_u32_e32 v148, v148, v193
	ds_read_b128 v[116:119], v148
	ds_read_b128 v[120:123], v149
	ds_read_b128 v[124:127], v148 offset:2048
	ds_read_b128 v[128:131], v149 offset:2048
	ds_read_b128 v[132:135], v148 offset:4096
	ds_read_b128 v[136:139], v149 offset:4096
	ds_read_b128 v[140:143], v148 offset:6144
	ds_read_b128 v[144:147], v149 offset:6144
	s_add_i32 s32, s1, 0x2000
	s_and_b32 s32, s32, 0x6000
	v_add_u32_e32 v208, s32, v192
	v_add_u32_e32 v209, v208, v195
	v_add_u32_e32 v208, v208, v193
	ds_read_b128 v[38:41], v208
	ds_read_b128 v[42:45], v209
	ds_read_b128 v[46:49], v208 offset:2048
	ds_read_b128 v[50:53], v209 offset:2048
	s_waitcnt lgkmcnt(12)
	v_sub_f32_e32 v81, v81, v199
	v_sub_f32_e32 v82, v82, v199
	v_mov_b32_e32 v70, v81
	v_mov_b32_e32 v71, v81
	v_mov_b32_e32 v72, v81
	v_mov_b32_e32 v73, v81
	v_mov_b32_e32 v74, v81
	v_mov_b32_e32 v75, v81
	v_mov_b32_e32 v76, v81
	v_mov_b32_e32 v77, v81
	v_mov_b32_e32 v200, v81
	v_mov_b32_e32 v201, v81
	v_mov_b32_e32 v202, v81
	v_mov_b32_e32 v203, v81
	v_mov_b32_e32 v204, v81
	v_mov_b32_e32 v205, v81
	v_mov_b32_e32 v206, v81
	v_mov_b32_e32 v207, v81
	v_mov_b32_e32 v54, v82
	v_mov_b32_e32 v55, v82
	v_mov_b32_e32 v56, v82
	v_mov_b32_e32 v57, v82
	v_mov_b32_e32 v58, v82
	v_mov_b32_e32 v59, v82
	v_mov_b32_e32 v60, v82
	v_mov_b32_e32 v61, v82
	v_mov_b32_e32 v62, v82
	v_mov_b32_e32 v63, v82
	v_mov_b32_e32 v64, v82
	v_mov_b32_e32 v65, v82
	v_mov_b32_e32 v66, v82
	v_mov_b32_e32 v67, v82
	v_mov_b32_e32 v68, v82
	v_mov_b32_e32 v69, v82
	s_waitcnt lgkmcnt(10)
	v_mfma_f32_16x16x32_bf16 v[70:73], v[116:119], v[104:107], v[70:73]
	v_mfma_f32_16x16x32_bf16 v[70:73], v[120:123], v[108:111], v[70:73]
	s_waitcnt lgkmcnt(8)
	v_mfma_f32_16x16x32_bf16 v[74:77], v[124:127], v[104:107], v[74:77]
	v_mfma_f32_16x16x32_bf16 v[74:77], v[128:131], v[108:111], v[74:77]
	ds_read_b128 v[116:119], v148 offset:32768
	ds_read_b128 v[120:123], v149 offset:32768
	ds_read_b128 v[124:127], v148 offset:34816
	ds_read_b128 v[128:131], v149 offset:34816
	s_waitcnt lgkmcnt(10)
	v_mfma_f32_16x16x32_bf16 v[200:203], v[132:135], v[104:107], v[200:203]
	v_mfma_f32_16x16x32_bf16 v[200:203], v[136:139], v[108:111], v[200:203]
	s_waitcnt lgkmcnt(8)
	v_mfma_f32_16x16x32_bf16 v[204:207], v[140:143], v[104:107], v[204:207]
	v_mfma_f32_16x16x32_bf16 v[204:207], v[144:147], v[108:111], v[204:207]
	ds_read_b128 v[132:135], v148 offset:36864
	ds_read_b128 v[136:139], v149 offset:36864
	ds_read_b128 v[140:143], v148 offset:38912
	ds_read_b128 v[144:147], v149 offset:38912
	s_waitcnt lgkmcnt(10)
	v_mfma_f32_16x16x32_bf16 v[54:57], v[38:41], v[104:107], v[54:57]
	v_mfma_f32_16x16x32_bf16 v[54:57], v[42:45], v[108:111], v[54:57]
	s_waitcnt lgkmcnt(8)
	v_mfma_f32_16x16x32_bf16 v[58:61], v[46:49], v[104:107], v[58:61]
	v_mfma_f32_16x16x32_bf16 v[58:61], v[50:53], v[108:111], v[58:61]
	ds_read_b128 v[38:41], v208 offset:4096
	ds_read_b128 v[42:45], v209 offset:4096
	ds_read_b128 v[46:49], v208 offset:6144
	ds_read_b128 v[50:53], v209 offset:6144
	v_exp_f32_e32 v70, v70
	v_exp_f32_e32 v71, v71
	v_exp_f32_e32 v72, v72
	v_exp_f32_e32 v73, v73
	v_exp_f32_e32 v74, v74
	v_exp_f32_e32 v75, v75
	v_exp_f32_e32 v76, v76
	v_exp_f32_e32 v77, v77
	v_exp_f32_e32 v200, v200
	v_exp_f32_e32 v201, v201
	v_exp_f32_e32 v202, v202
	v_exp_f32_e32 v203, v203
	v_exp_f32_e32 v204, v204
	v_exp_f32_e32 v205, v205
	v_exp_f32_e32 v206, v206
	v_exp_f32_e32 v207, v207
	s_nop 0
	v_cvt_pk_bf16_f32 v70, v70, v71
	v_cvt_pk_bf16_f32 v71, v72, v73
	v_cvt_pk_bf16_f32 v72, v74, v75
	v_cvt_pk_bf16_f32 v73, v76, v77
	v_cvt_pk_bf16_f32 v74, v200, v201
	v_cvt_pk_bf16_f32 v75, v202, v203
	v_cvt_pk_bf16_f32 v76, v204, v205
	v_cvt_pk_bf16_f32 v77, v206, v207
	s_nop 1
	v_mfma_f32_16x16x32_bf16 v[100:103], v[112:115], v[70:73], 0
	v_mfma_f32_16x16x32_bf16 v[100:103], v[112:115], v[74:77], v[100:103]
	s_waitcnt lgkmcnt(4)
	v_mfma_f32_16x16x32_bf16 v[84:87], v[116:119], v[70:73], 0
	v_mfma_f32_16x16x32_bf16 v[84:87], v[120:123], v[74:77], v[84:87]
	v_mfma_f32_16x16x32_bf16 v[88:91], v[124:127], v[70:73], 0
	v_mfma_f32_16x16x32_bf16 v[88:91], v[128:131], v[74:77], v[88:91]
	v_mfma_f32_16x16x32_bf16 v[92:95], v[132:135], v[70:73], 0
	v_mfma_f32_16x16x32_bf16 v[92:95], v[136:139], v[74:77], v[92:95]
	v_mfma_f32_16x16x32_bf16 v[96:99], v[140:143], v[70:73], 0
	v_mfma_f32_16x16x32_bf16 v[96:99], v[144:147], v[74:77], v[96:99]
	s_waitcnt lgkmcnt(2)
	v_mfma_f32_16x16x32_bf16 v[62:65], v[38:41], v[104:107], v[62:65]
	v_mfma_f32_16x16x32_bf16 v[62:65], v[42:45], v[108:111], v[62:65]
	s_waitcnt lgkmcnt(0)
	v_mfma_f32_16x16x32_bf16 v[66:69], v[46:49], v[104:107], v[66:69]
	v_mfma_f32_16x16x32_bf16 v[66:69], v[50:53], v[108:111], v[66:69]
	ds_read_b128 v[116:119], v208 offset:32768
	ds_read_b128 v[120:123], v209 offset:32768
	ds_read_b128 v[124:127], v208 offset:34816
	ds_read_b128 v[128:131], v209 offset:34816
	ds_read_b128 v[132:135], v208 offset:36864
	ds_read_b128 v[136:139], v209 offset:36864
	ds_read_b128 v[140:143], v208 offset:38912
	ds_read_b128 v[144:147], v209 offset:38912
	s_nop 3
	v_exp_f32_e32 v54, v54
	v_exp_f32_e32 v55, v55
	v_exp_f32_e32 v56, v56
	v_exp_f32_e32 v57, v57
	v_exp_f32_e32 v58, v58
	v_exp_f32_e32 v59, v59
	v_exp_f32_e32 v60, v60
	v_exp_f32_e32 v61, v61
	v_exp_f32_e32 v62, v62
	v_exp_f32_e32 v63, v63
	v_exp_f32_e32 v64, v64
	v_exp_f32_e32 v65, v65
	v_exp_f32_e32 v66, v66
	v_exp_f32_e32 v67, v67
	v_exp_f32_e32 v68, v68
	v_exp_f32_e32 v69, v69
	s_nop 0
	v_cvt_pk_bf16_f32 v54, v54, v55
	v_cvt_pk_bf16_f32 v55, v56, v57
	v_cvt_pk_bf16_f32 v56, v58, v59
	v_cvt_pk_bf16_f32 v57, v60, v61
	v_cvt_pk_bf16_f32 v58, v62, v63
	v_cvt_pk_bf16_f32 v59, v64, v65
	v_cvt_pk_bf16_f32 v60, v66, v67
	v_cvt_pk_bf16_f32 v61, v68, v69
	s_nop 1
	v_mfma_f32_16x16x32_bf16 v[100:103], v[112:115], v[54:57], v[100:103]
	v_mfma_f32_16x16x32_bf16 v[100:103], v[112:115], v[58:61], v[100:103]
	s_waitcnt lgkmcnt(4)
; template <bool SELMASK>
; __device__ __forceinline__ void attn_far_fast(const LAS unsigned char* kb, const LAS unsigned char* vb, const bf16x8 (&qf)[2][2], int col, int q, float bias_far, bool sel0, bool sel1, Softmax (&st)[2], f32x4 (&O)[2][4]) {
;     ...
; #pragma unroll
;     for (int c32 = 0; c32 < 2; ++c32)
; #pragma unroll
;         for (int dt = 0; dt < 4; ++dt) { const bf16x8 vf = lds_frag(vb, 16 * dt + col, 4 * c32 + q);
;             O[0][dt] = __builtin_amdgcn_mfma_f32_16x16x32_bf16(vf, pf[0][c32], O[0][dt], 0, 0, 0);
;             O[1][dt] = __builtin_amdgcn_mfma_f32_16x16x32_bf16(vf, pf[1][c32], O[1][dt], 0, 0, 0); }
	v_mfma_f32_16x16x32_bf16 v[84:87], v[116:119], v[54:57], v[84:87]
	v_mfma_f32_16x16x32_bf16 v[84:87], v[120:123], v[58:61], v[84:87]
	v_mfma_f32_16x16x32_bf16 v[88:91], v[124:127], v[54:57], v[88:91]
	v_mfma_f32_16x16x32_bf16 v[88:91], v[128:131], v[58:61], v[88:91]
	v_lshlrev_b32_e32 v254, 6, v186
	v_sub_u32_e32 v254, v83, v254
	ds_read2_b32 v[200:201], v83 offset0:0 offset1:4
	ds_read2_b32 v[202:203], v83 offset0:8 offset1:12
	ds_read2_b32 v[204:205], v83 offset0:64 offset1:68
	ds_read2_b32 v[206:207], v83 offset0:72 offset1:76
	ds_read2_b32 v[62:63], v83 offset0:128 offset1:132
	ds_read2_b32 v[64:65], v83 offset0:136 offset1:140
	ds_read2_b32 v[66:67], v83 offset0:192 offset1:196
	ds_read2_b32 v[68:69], v83 offset0:200 offset1:204
	ds_read_b32 v199, v254 offset:1024
	s_waitcnt lgkmcnt(9)
	v_mfma_f32_16x16x32_bf16 v[92:95], v[132:135], v[54:57], v[92:95]
	v_mfma_f32_16x16x32_bf16 v[92:95], v[136:139], v[58:61], v[92:95]
	v_mfma_f32_16x16x32_bf16 v[96:99], v[140:143], v[54:57], v[96:99]
	v_mfma_f32_16x16x32_bf16 v[96:99], v[144:147], v[58:61], v[96:99]
	s_nop 1
	s_waitcnt lgkmcnt(0)
	v_add_f32_e32 v200, v200, v84
	v_add_f32_e32 v201, v201, v85
	v_add_f32_e32 v202, v202, v86
	v_add_f32_e32 v203, v203, v87
	v_add_f32_e32 v204, v204, v88
	v_add_f32_e32 v205, v205, v89
	v_add_f32_e32 v206, v206, v90
	v_add_f32_e32 v207, v207, v91
	v_add_f32_e32 v199, v199, v100
	v_add_f32_e32 v62, v62, v92
	v_add_f32_e32 v63, v63, v93
	v_add_f32_e32 v64, v64, v94
	v_add_f32_e32 v65, v65, v95
	v_add_f32_e32 v66, v66, v96
	v_add_f32_e32 v67, v67, v97
	v_add_f32_e32 v68, v68, v98
	v_add_f32_e32 v69, v69, v99
	v_cmp_ne_u32_e32 vcc, 0, v79
	s_and_saveexec_b64 s[84:85], vcc
	ds_write2_b32 v83, v200, v201 offset0:0 offset1:4
	ds_write2_b32 v83, v202, v203 offset0:8 offset1:12
	ds_write2_b32 v83, v204, v205 offset0:64 offset1:68
	ds_write2_b32 v83, v206, v207 offset0:72 offset1:76
	ds_write2_b32 v83, v62, v63 offset0:128 offset1:132
	ds_write2_b32 v83, v64, v65 offset0:136 offset1:140
	ds_write2_b32 v83, v66, v67 offset0:192 offset1:196
	ds_write2_b32 v83, v68, v69 offset0:200 offset1:204
	ds_write_b32 v254, v199 offset:1024
	s_mov_b64 exec, s[84:85]
	s_nop 3
	s_mov_b32 s100, -1
	s_add_i32 s21, s91, 8
	s_lshr_b32 s77, s75, 1
	s_and_b32 s77, s77, 3
	s_mul_i32 s77, s77, 80
	s_add_i32 s77, s77, 0x20900
	s_lshl_b32 s32, s21, 2
	v_lshrrev_b32_e32 v58, 2, v250
	v_add_u32_e32 v58, s32, v58
	v_mov_b32_e32 v59, s77
	v_add_u32_e32 v63, s77, v58
	ds_read_u8 v59, v59 offset:64
	ds_read_u8 v63, v63
	s_waitcnt lgkmcnt(0)
	v_readfirstlane_b32 s11, v59
	s_nop 3
	v_cmp_gt_u32_e32 vcc, s11, v58
	s_nop 1
	v_cndmask_b32_e32 v63, -1, v63, vcc
	v_lshrrev_b32_e32 v56, 31, v63
	v_xor_b32_e32 v56, 1, v56
	v_max_i32_e32 v55, 0, v63
	v_mov_b32_e32 v79, v56
	v_and_b32_e32 v54, 63, v55
	v_bfe_u32 v58, v55, 6, 1
	v_bfe_u32 v59, v55, 7, 1
	v_lshlrev_b32_e32 v60, 11, v54
	v_mov_b32_e32 v61, 0
	v_lshl_add_u64 v[60:61], v[60:61], 0, v[246:247]
	global_load_dwordx4 v[104:107], v[60:61], off
	global_load_dwordx4 v[108:111], v[60:61], off offset:64
	v_lshl_add_u32 v63, v54, 4, v249
	ds_read_b32 v199, v63
	v_mul_u32_u24_e32 v83, 0x410, v54
	v_cmp_ne_u32_e32 vcc, 0, v58
	v_add_u32_e32 v83, v83, v248
	s_nop 0
	v_cndmask_b32_e32 v81, v2, v154, vcc
	s_cmp_lg_u64 vcc, 0
	s_cselect_b32 s21, 1, 0
	v_cmp_ne_u32_e32 vcc, 0, v59
	s_nop 1
	v_cndmask_b32_e32 v82, v2, v154, vcc
	s_cmp_lg_u64 vcc, 0
	s_cselect_b32 s32, 1, 0
	s_waitcnt vmcnt(0)
	s_and_b32 s83, s1, 0x4000
	v_add_u32_e32 v148, s83, v192
	v_add_u32_e32 v149, v148, v195
	v_add_u32_e32 v148, v148, v193
	ds_read_b128 v[116:119], v148
	ds_read_b128 v[120:123], v149
	ds_read_b128 v[124:127], v148 offset:2048
	ds_read_b128 v[128:131], v149 offset:2048
	ds_read_b128 v[132:135], v148 offset:4096
	ds_read_b128 v[136:139], v149 offset:4096
	ds_read_b128 v[140:143], v148 offset:6144
	ds_read_b128 v[144:147], v149 offset:6144
	s_add_i32 s32, s1, 0x2000
	s_and_b32 s32, s32, 0x6000
	v_add_u32_e32 v208, s32, v192
	v_add_u32_e32 v209, v208, v195
	v_add_u32_e32 v208, v208, v193
	ds_read_b128 v[38:41], v208
	ds_read_b128 v[42:45], v209
	ds_read_b128 v[46:49], v208 offset:2048
	ds_read_b128 v[50:53], v209 offset:2048
	s_waitcnt lgkmcnt(12)
	v_sub_f32_e32 v81, v81, v199
	v_sub_f32_e32 v82, v82, v199
	v_mov_b32_e32 v70, v81
	v_mov_b32_e32 v71, v81
	v_mov_b32_e32 v72, v81
	v_mov_b32_e32 v73, v81
	v_mov_b32_e32 v74, v81
	v_mov_b32_e32 v75, v81
	v_mov_b32_e32 v76, v81
	v_mov_b32_e32 v77, v81
	v_mov_b32_e32 v200, v81
	v_mov_b32_e32 v201, v81
	v_mov_b32_e32 v202, v81
	v_mov_b32_e32 v203, v81
	v_mov_b32_e32 v204, v81
	v_mov_b32_e32 v205, v81
	v_mov_b32_e32 v206, v81
	v_mov_b32_e32 v207, v81
	v_mov_b32_e32 v54, v82
	v_mov_b32_e32 v55, v82
	v_mov_b32_e32 v56, v82
	v_mov_b32_e32 v57, v82
	v_mov_b32_e32 v58, v82
	v_mov_b32_e32 v59, v82
	v_mov_b32_e32 v60, v82
	v_mov_b32_e32 v61, v82
	v_mov_b32_e32 v62, v82
	v_mov_b32_e32 v63, v82
	v_mov_b32_e32 v64, v82
	v_mov_b32_e32 v65, v82
	v_mov_b32_e32 v66, v82
	v_mov_b32_e32 v67, v82
	v_mov_b32_e32 v68, v82
	v_mov_b32_e32 v69, v82
	s_waitcnt lgkmcnt(10)
	v_mfma_f32_16x16x32_bf16 v[70:73], v[116:119], v[104:107], v[70:73]
	v_mfma_f32_16x16x32_bf16 v[70:73], v[120:123], v[108:111], v[70:73]
	s_waitcnt lgkmcnt(8)
	v_mfma_f32_16x16x32_bf16 v[74:77], v[124:127], v[104:107], v[74:77]
	v_mfma_f32_16x16x32_bf16 v[74:77], v[128:131], v[108:111], v[74:77]
	ds_read_b128 v[116:119], v148 offset:32768
	ds_read_b128 v[120:123], v149 offset:32768
	ds_read_b128 v[124:127], v148 offset:34816
	ds_read_b128 v[128:131], v149 offset:34816
	s_waitcnt lgkmcnt(10)
	v_mfma_f32_16x16x32_bf16 v[200:203], v[132:135], v[104:107], v[200:203]
	v_mfma_f32_16x16x32_bf16 v[200:203], v[136:139], v[108:111], v[200:203]
	s_waitcnt lgkmcnt(8)
; __device__ __forceinline__ float ex2(float x) { return __builtin_amdgcn_exp2f(x); }
; template <bool SELMASK>
; __device__ __forceinline__ void attn_far_fast(const LAS unsigned char* kb, const LAS unsigned char* vb, const bf16x8 (&qf)[2][2], int col, int q, float bias_far, bool sel0, bool sel1, Softmax (&st)[2], f32x4 (&O)[2][4]) {
;     ...
; #pragma unroll
;     for (int kt = 0; kt < 4; ++kt) { const bf16x8 k0 = lds_frag(kb, 16 * kt + col, q), k1 = lds_frag(kb, 16 * kt + col, 4 + q);
; #pragma unroll
;         for (int c = 0; c < 2; ++c) { S[c][kt] = __builtin_amdgcn_mfma_f32_16x16x32_bf16(k0, qf[c][0], z4, 0, 0, 0); S[c][kt] = __builtin_amdgcn_mfma_f32_16x16x32_bf16(k1, qf[c][1], S[c][kt], 0, 0, 0); } }
;     bf16x8 pf[2][2];
; #pragma unroll
;     for (int c = 0; c < 2; ++c) {
;         const bool sel = c == 0 ? sel0 : sel1;
;         const float off = ((SELMASK && !sel) ? NEG : bias_far) - st[c].m;
; #pragma unroll
;         for (int kt = 0; kt < 4; ++kt) { f32x4 p = S[c][kt] + off;
; #pragma unroll
;             for (int e = 0; e < 4; ++e) p[e] = ex2(p[e]);
;             S[c][kt] = p; }
;         pf[c][0] = pack8(S[c][0], S[c][1]); pf[c][1] = pack8(S[c][2], S[c][3]);
;         st[c].l = __builtin_amdgcn_mfma_f32_16x16x32_bf16(ONES8, pf[c][0], st[c].l, 0, 0, 0); st[c].l = __builtin_amdgcn_mfma_f32_16x16x32_bf16(ONES8, pf[c][1], st[c].l, 0, 0, 0);
;     }
; #pragma unroll
;     for (int c32 = 0; c32 < 2; ++c32)
; #pragma unroll
;         for (int dt = 0; dt < 4; ++dt) { const bf16x8 vf = lds_frag(vb, 16 * dt + col, 4 * c32 + q);
;             O[0][dt] = __builtin_amdgcn_mfma_f32_16x16x32_bf16(vf, pf[0][c32], O[0][dt], 0, 0, 0);
;             O[1][dt] = __builtin_amdgcn_mfma_f32_16x16x32_bf16(vf, pf[1][c32], O[1][dt], 0, 0, 0); }
	v_mfma_f32_16x16x32_bf16 v[204:207], v[140:143], v[104:107], v[204:207]
	v_mfma_f32_16x16x32_bf16 v[204:207], v[144:147], v[108:111], v[204:207]
	ds_read_b128 v[132:135], v148 offset:36864
	ds_read_b128 v[136:139], v149 offset:36864
	ds_read_b128 v[140:143], v148 offset:38912
	ds_read_b128 v[144:147], v149 offset:38912
	s_waitcnt lgkmcnt(10)
	v_mfma_f32_16x16x32_bf16 v[54:57], v[38:41], v[104:107], v[54:57]
	v_mfma_f32_16x16x32_bf16 v[54:57], v[42:45], v[108:111], v[54:57]
	s_waitcnt lgkmcnt(8)
	v_mfma_f32_16x16x32_bf16 v[58:61], v[46:49], v[104:107], v[58:61]
	v_mfma_f32_16x16x32_bf16 v[58:61], v[50:53], v[108:111], v[58:61]
	ds_read_b128 v[38:41], v208 offset:4096
	ds_read_b128 v[42:45], v209 offset:4096
	ds_read_b128 v[46:49], v208 offset:6144
	ds_read_b128 v[50:53], v209 offset:6144
	v_exp_f32_e32 v70, v70
	v_exp_f32_e32 v71, v71
	v_exp_f32_e32 v72, v72
	v_exp_f32_e32 v73, v73
	v_exp_f32_e32 v74, v74
	v_exp_f32_e32 v75, v75
	v_exp_f32_e32 v76, v76
	v_exp_f32_e32 v77, v77
	v_exp_f32_e32 v200, v200
	v_exp_f32_e32 v201, v201
	v_exp_f32_e32 v202, v202
	v_exp_f32_e32 v203, v203
	v_exp_f32_e32 v204, v204
	v_exp_f32_e32 v205, v205
	v_exp_f32_e32 v206, v206
	v_exp_f32_e32 v207, v207
	s_nop 0
	v_cvt_pk_bf16_f32 v70, v70, v71
	v_cvt_pk_bf16_f32 v71, v72, v73
	v_cvt_pk_bf16_f32 v72, v74, v75
	v_cvt_pk_bf16_f32 v73, v76, v77
	v_cvt_pk_bf16_f32 v74, v200, v201
	v_cvt_pk_bf16_f32 v75, v202, v203
	v_cvt_pk_bf16_f32 v76, v204, v205
	v_cvt_pk_bf16_f32 v77, v206, v207
	s_nop 1
	v_mfma_f32_16x16x32_bf16 v[100:103], v[112:115], v[70:73], 0
	v_mfma_f32_16x16x32_bf16 v[100:103], v[112:115], v[74:77], v[100:103]
	s_waitcnt lgkmcnt(4)
	v_mfma_f32_16x16x32_bf16 v[84:87], v[116:119], v[70:73], 0
	v_mfma_f32_16x16x32_bf16 v[84:87], v[120:123], v[74:77], v[84:87]
	v_mfma_f32_16x16x32_bf16 v[88:91], v[124:127], v[70:73], 0
	v_mfma_f32_16x16x32_bf16 v[88:91], v[128:131], v[74:77], v[88:91]
	v_mfma_f32_16x16x32_bf16 v[92:95], v[132:135], v[70:73], 0
	v_mfma_f32_16x16x32_bf16 v[92:95], v[136:139], v[74:77], v[92:95]
	v_mfma_f32_16x16x32_bf16 v[96:99], v[140:143], v[70:73], 0
	v_mfma_f32_16x16x32_bf16 v[96:99], v[144:147], v[74:77], v[96:99]
	s_waitcnt lgkmcnt(2)
	v_mfma_f32_16x16x32_bf16 v[62:65], v[38:41], v[104:107], v[62:65]
	v_mfma_f32_16x16x32_bf16 v[62:65], v[42:45], v[108:111], v[62:65]
	s_waitcnt lgkmcnt(0)
	v_mfma_f32_16x16x32_bf16 v[66:69], v[46:49], v[104:107], v[66:69]
	v_mfma_f32_16x16x32_bf16 v[66:69], v[50:53], v[108:111], v[66:69]
	ds_read_b128 v[116:119], v208 offset:32768
	ds_read_b128 v[120:123], v209 offset:32768
	ds_read_b128 v[124:127], v208 offset:34816
	ds_read_b128 v[128:131], v209 offset:34816
	ds_read_b128 v[132:135], v208 offset:36864
	ds_read_b128 v[136:139], v209 offset:36864
	ds_read_b128 v[140:143], v208 offset:38912
	ds_read_b128 v[144:147], v209 offset:38912
	s_nop 3
	v_exp_f32_e32 v54, v54
	v_exp_f32_e32 v55, v55
	v_exp_f32_e32 v56, v56
	v_exp_f32_e32 v57, v57
	v_exp_f32_e32 v58, v58
	v_exp_f32_e32 v59, v59
	v_exp_f32_e32 v60, v60
	v_exp_f32_e32 v61, v61
	v_exp_f32_e32 v62, v62
	v_exp_f32_e32 v63, v63
	v_exp_f32_e32 v64, v64
	v_exp_f32_e32 v65, v65
	v_exp_f32_e32 v66, v66
	v_exp_f32_e32 v67, v67
	v_exp_f32_e32 v68, v68
	v_exp_f32_e32 v69, v69
	s_nop 0
	v_cvt_pk_bf16_f32 v54, v54, v55
	v_cvt_pk_bf16_f32 v55, v56, v57
	v_cvt_pk_bf16_f32 v56, v58, v59
	v_cvt_pk_bf16_f32 v57, v60, v61
	v_cvt_pk_bf16_f32 v58, v62, v63
	v_cvt_pk_bf16_f32 v59, v64, v65
	v_cvt_pk_bf16_f32 v60, v66, v67
	v_cvt_pk_bf16_f32 v61, v68, v69
	s_nop 1
	v_mfma_f32_16x16x32_bf16 v[100:103], v[112:115], v[54:57], v[100:103]
	v_mfma_f32_16x16x32_bf16 v[100:103], v[112:115], v[58:61], v[100:103]
	s_waitcnt lgkmcnt(4)
	v_mfma_f32_16x16x32_bf16 v[84:87], v[116:119], v[54:57], v[84:87]
	v_mfma_f32_16x16x32_bf16 v[84:87], v[120:123], v[58:61], v[84:87]
	v_mfma_f32_16x16x32_bf16 v[88:91], v[124:127], v[54:57], v[88:91]
	v_mfma_f32_16x16x32_bf16 v[88:91], v[128:131], v[58:61], v[88:91]
	v_lshlrev_b32_e32 v254, 6, v186
	v_sub_u32_e32 v254, v83, v254
	ds_read2_b32 v[200:201], v83 offset0:0 offset1:4
	ds_read2_b32 v[202:203], v83 offset0:8 offset1:12
	ds_read2_b32 v[204:205], v83 offset0:64 offset1:68
	ds_read2_b32 v[206:207], v83 offset0:72 offset1:76
	ds_read2_b32 v[62:63], v83 offset0:128 offset1:132
	ds_read2_b32 v[64:65], v83 offset0:136 offset1:140
	ds_read2_b32 v[66:67], v83 offset0:192 offset1:196
	ds_read2_b32 v[68:69], v83 offset0:200 offset1:204
	ds_read_b32 v199, v254 offset:1024
	s_waitcnt lgkmcnt(9)
	v_mfma_f32_16x16x32_bf16 v[92:95], v[132:135], v[54:57], v[92:95]
	v_mfma_f32_16x16x32_bf16 v[92:95], v[136:139], v[58:61], v[92:95]
	v_mfma_f32_16x16x32_bf16 v[96:99], v[140:143], v[54:57], v[96:99]
	v_mfma_f32_16x16x32_bf16 v[96:99], v[144:147], v[58:61], v[96:99]
	s_nop 1
	s_waitcnt lgkmcnt(0)
	v_add_f32_e32 v200, v200, v84
	v_add_f32_e32 v201, v201, v85
	v_add_f32_e32 v202, v202, v86
	v_add_f32_e32 v203, v203, v87
	v_add_f32_e32 v204, v204, v88
	v_add_f32_e32 v205, v205, v89
	v_add_f32_e32 v206, v206, v90
	v_add_f32_e32 v207, v207, v91
	v_add_f32_e32 v199, v199, v100
	v_add_f32_e32 v62, v62, v92
	v_add_f32_e32 v63, v63, v93
	v_add_f32_e32 v64, v64, v94
	v_add_f32_e32 v65, v65, v95
	v_add_f32_e32 v66, v66, v96
	v_add_f32_e32 v67, v67, v97
	v_add_f32_e32 v68, v68, v98
	v_add_f32_e32 v69, v69, v99
	v_cmp_ne_u32_e32 vcc, 0, v79
	s_and_saveexec_b64 s[84:85], vcc
	ds_write2_b32 v83, v200, v201 offset0:0 offset1:4
	ds_write2_b32 v83, v202, v203 offset0:8 offset1:12
	ds_write2_b32 v83, v204, v205 offset0:64 offset1:68
	ds_write2_b32 v83, v206, v207 offset0:72 offset1:76
	ds_write2_b32 v83, v62, v63 offset0:128 offset1:132
	ds_write2_b32 v83, v64, v65 offset0:136 offset1:140
	ds_write2_b32 v83, v66, v67 offset0:192 offset1:196
	ds_write2_b32 v83, v68, v69 offset0:200 offset1:204
	ds_write_b32 v254, v199 offset:1024
	s_mov_b64 exec, s[84:85]
	s_nop 3

.Lbm_noitem:
	s_mov_b32 s83, -1
	s_add_i32 s77, s75, 2
	s_cmp_gt_i32 s77, s26
	s_cbranch_scc1 .Lbm_g1_end_nb
	s_lshr_b32 s77, s77, 1
	s_and_b32 s77, s77, 3
	s_mul_i32 s77, s77, 80
	s_add_i32 s77, s77, 0x20900
	s_lshl_b32 s32, s91, 2
	v_lshrrev_b32_e32 v78, 2, v250
	v_add_u32_e32 v78, s32, v78
	v_mov_b32_e32 v255, s77
	v_add_u32_e32 v254, s77, v78
	ds_read_u8 v255, v255 offset:64
	ds_read_u8 v251, v254
	s_mov_b32 s83, 0
.Lbm_g1_end_nb:
	s_mov_b32 s100, -1
	s_cmp_lt_i32 s83, 0
	s_cbranch_scc1 .Lbm_g2_end_nb
	s_waitcnt lgkmcnt(0)
	v_readfirstlane_b32 s11, v255
	s_add_i32 s32, s11, 3
	s_lshr_b32 s32, s32, 2
	s_cmp_ge_u32 s91, s32
	s_cbranch_scc1 .Lbm_g2_end_nb
	v_cmp_gt_u32_e32 vcc, s11, v78
	s_add_i32 s83, s91, 8
	s_cmp_lt_u32 s83, s32
	s_cselect_b32 s83, 0x10000, 0
	s_add_i32 s83, s83, s75
	s_add_i32 s83, s83, 2
	v_cndmask_b32_e32 v251, -1, v251, vcc
	v_max_i32_e32 v254, 0, v251
	v_and_b32_e32 v254, 63, v254
	v_lshlrev_b32_e32 v254, 11, v254
	v_mov_b32_e32 v255, 0
	v_lshl_add_u64 v[254:255], v[254:255], 0, v[246:247]
	global_load_dwordx4 v[104:107], v[254:255], off
	global_load_dwordx4 v[108:111], v[254:255], off offset:64
	s_mov_b32 s100, s83
